# attention unit epilogues (MoBA, forgetting, stick-breaking) and pool epilogue: half-wave exchange with v_permlane32_swap so each lane stores 16 bytes (4 stores per unit instead of 8; 8 per pool task i
# speedup vs baseline: 1.0108x; 1.0108x over previous
; __device__ __forceinline__ unsigned pk2(float lo, float hi) { const f32x2_pk v = {lo, hi}; return __builtin_bit_cast(unsigned, __builtin_convertvector(v, bf16x2)); }
; __device__ __forceinline__ void attn_fox_unit(Frame& F, const bf16_t* Qh, const bf16_t* Kh, const bf16_t* Vth, const float* CFh, const int qb, bf16_t* AOp, const float k2max) {
;     ...
;     const float linv = 1.f / (l + __shfl_xor(l, 32));
;     bf16_t* orow = AOp + (size_t)q * DM;
; #pragma unroll
;     for (int g = 0; g < 4; ++g) { u32x2 w;
;         w.x = pk2(O0[4 * g] * linv, O0[4 * g + 1] * linv); w.y = pk2(O0[4 * g + 2] * linv, O0[4 * g + 3] * linv); *(u32x2*)(orow + 8 * g + 4 * hi) = w;
;         w.x = pk2(O1[4 * g] * linv, O1[4 * g + 1] * linv); w.y = pk2(O1[4 * g + 2] * linv, O1[4 * g + 3] * linv); *(u32x2*)(orow + 32 + 8 * g + 4 * hi) = w; }
.LBB0_533:
	ds_bpermute_b32 v35, v146, v151
	v_lshlrev_b64 v[32:33], 11, v[114:115]
	v_lshlrev_b32_e32 v34, 3, v148
	s_add_i32 s87, s87, 1
	s_cmp_eq_u32 s87, 4
	s_waitcnt lgkmcnt(0)
	v_add_f32_e32 v35, v151, v35
	v_div_scale_f32 v36, s[0:1], v35, v35, 1.0
	v_rcp_f32_e32 v37, v36
	v_div_scale_f32 v38, vcc, 1.0, v35, 1.0
	v_readlane_b32 s0, v236, 35
	v_fma_f32 v39, -v36, v37, 1.0
	v_fmac_f32_e32 v37, v39, v37
	v_mul_f32_e32 v39, v38, v37
	v_fma_f32 v40, -v36, v39, v38
	v_fmac_f32_e32 v39, v40, v37
	v_fma_f32 v36, -v36, v39, v38
	v_div_fmas_f32 v36, v36, v37, v39
	v_readlane_b32 s1, v236, 36
	v_div_fixup_f32 v36, v36, v35, 1.0
	v_ashrrev_i32_e32 v35, 31, v34
	v_lshl_add_u64 v[32:33], s[0:1], 0, v[32:33]
	v_lshl_add_u64 v[32:33], v[34:35], 1, v[32:33]
	v_pk_mul_f32 v[0:1], v[0:1], v[36:37] op_sel_hi:[1,0]
	v_pk_mul_f32 v[2:3], v[2:3], v[36:37] op_sel_hi:[1,0]
	v_pk_mul_f32 v[4:5], v[4:5], v[36:37] op_sel_hi:[1,0]
	v_pk_mul_f32 v[6:7], v[6:7], v[36:37] op_sel_hi:[1,0]
	v_pk_mul_f32 v[8:9], v[8:9], v[36:37] op_sel_hi:[1,0]
	v_pk_mul_f32 v[10:11], v[10:11], v[36:37] op_sel_hi:[1,0]
	v_pk_mul_f32 v[12:13], v[12:13], v[36:37] op_sel_hi:[1,0]
	v_pk_mul_f32 v[14:15], v[14:15], v[36:37] op_sel_hi:[1,0]
	v_pk_mul_f32 v[16:17], v[16:17], v[36:37] op_sel_hi:[1,0]
	v_pk_mul_f32 v[18:19], v[18:19], v[36:37] op_sel_hi:[1,0]
	v_pk_mul_f32 v[20:21], v[20:21], v[36:37] op_sel_hi:[1,0]
	v_pk_mul_f32 v[22:23], v[22:23], v[36:37] op_sel_hi:[1,0]
	v_pk_mul_f32 v[24:25], v[24:25], v[36:37] op_sel_hi:[1,0]
	v_pk_mul_f32 v[26:27], v[26:27], v[36:37] op_sel_hi:[1,0]
	v_pk_mul_f32 v[28:29], v[28:29], v[36:37] op_sel_hi:[1,0]
	v_pk_mul_f32 v[30:31], v[30:31], v[36:37] op_sel_hi:[1,0]
	v_cvt_pk_bf16_f32 v0, v0, v1
	v_cvt_pk_bf16_f32 v1, v2, v3
	v_cvt_pk_bf16_f32 v2, v4, v5
	v_cvt_pk_bf16_f32 v3, v6, v7
	v_cvt_pk_bf16_f32 v4, v8, v9
	v_cvt_pk_bf16_f32 v5, v10, v11
	v_cvt_pk_bf16_f32 v6, v12, v13
	v_cvt_pk_bf16_f32 v7, v14, v15
	v_cvt_pk_bf16_f32 v16, v16, v17
	v_cvt_pk_bf16_f32 v17, v18, v19
	v_cvt_pk_bf16_f32 v18, v20, v21
	v_cvt_pk_bf16_f32 v19, v22, v23
	v_cvt_pk_bf16_f32 v20, v24, v25
	v_cvt_pk_bf16_f32 v21, v26, v27
	v_cvt_pk_bf16_f32 v22, v28, v29
	v_cvt_pk_bf16_f32 v23, v30, v31
	s_nop 1
	v_permlane32_swap_b32_e32 v0, v2
	v_permlane32_swap_b32_e32 v1, v3
	v_permlane32_swap_b32_e32 v4, v6
	v_permlane32_swap_b32_e32 v5, v7
	v_permlane32_swap_b32_e32 v16, v18
	v_permlane32_swap_b32_e32 v17, v19
	v_permlane32_swap_b32_e32 v20, v22
	v_permlane32_swap_b32_e32 v21, v23
	global_store_dwordx4 v[32:33], v[0:3], off
	global_store_dwordx4 v[32:33], v[4:7], off offset:32
	global_store_dwordx4 v[32:33], v[16:19], off offset:64
	global_store_dwordx4 v[32:33], v[20:23], off offset:96
	s_waitcnt vmcnt(0) lgkmcnt(0)
	s_barrier
	s_cbranch_scc1 .LBB0_510

; __device__ __forceinline__ unsigned pk2(float lo, float hi) { const f32x2_pk v = {lo, hi}; return __builtin_bit_cast(unsigned, __builtin_convertvector(v, bf16x2)); }
; template <int KIND>
; __device__ __forceinline__ void attn_wave(const bf16_t* Qh, const bf16_t* Kh, const bf16_t* Vth, const int q0, const int lane, const float* CFh, const float slope2, const float* KMh, bf16_t* AOp) {
;     ...
;     float linv = 1.f;
;     if (KIND != 1) linv = 1.f / (l + __shfl_xor(l, 32));
;     bf16_t* orow = AOp + (size_t)q * DM;
; #pragma unroll
;     for (int g = 0; g < 4; ++g) { u32x2 w;
;         w.x = pk2(O0[4 * g] * linv, O0[4 * g + 1] * linv); w.y = pk2(O0[4 * g + 2] * linv, O0[4 * g + 3] * linv); *(u32x2*)(orow + 8 * g + 4 * hi) = w;
;         w.x = pk2(O1[4 * g] * linv, O1[4 * g + 1] * linv); w.y = pk2(O1[4 * g + 2] * linv, O1[4 * g + 3] * linv); *(u32x2*)(orow + 32 + 8 * g + 4 * hi) = w; }
.LBB0_572:
	s_lshl_b32 s0, s27, 18
	v_readlane_b32 s2, v237, 45
	s_and_b32 s0, s0, 0x3c00000
	v_readlane_b32 s3, v237, 46
	s_add_u32 s0, s2, s0
	s_addc_u32 s1, s3, 0
	s_lshl_b32 s2, s28, 7
	s_add_u32 s0, s0, s2
	s_addc_u32 s1, s1, 0
	v_lshlrev_b64 v[0:1], 11, v[130:131]
	v_lshlrev_b32_e32 v2, 3, v141
	v_lshl_add_u64 v[0:1], s[0:1], 0, v[0:1]
	v_ashrrev_i32_e32 v3, 31, v2
	v_lshl_add_u64 v[0:1], v[2:3], 1, v[0:1]
	s_mov_b64 s[0:1], 0
	v_cvt_pk_bf16_f32 v32, v32, v33
	v_cvt_pk_bf16_f32 v33, v34, v35
	v_cvt_pk_bf16_f32 v34, v36, v37
	v_cvt_pk_bf16_f32 v35, v38, v39
	v_cvt_pk_bf16_f32 v36, v40, v41
	v_cvt_pk_bf16_f32 v37, v42, v43
	v_cvt_pk_bf16_f32 v38, v44, v45
	v_cvt_pk_bf16_f32 v39, v46, v47
	v_cvt_pk_bf16_f32 v48, v48, v49
	v_cvt_pk_bf16_f32 v49, v50, v51
	v_cvt_pk_bf16_f32 v50, v52, v53
	v_cvt_pk_bf16_f32 v51, v54, v55
	v_cvt_pk_bf16_f32 v52, v56, v57
	v_cvt_pk_bf16_f32 v53, v58, v59
	v_cvt_pk_bf16_f32 v54, v60, v61
	v_cvt_pk_bf16_f32 v55, v62, v63
	s_nop 1
	v_permlane32_swap_b32_e32 v32, v34
	v_permlane32_swap_b32_e32 v33, v35
	v_permlane32_swap_b32_e32 v36, v38
	v_permlane32_swap_b32_e32 v37, v39
	v_permlane32_swap_b32_e32 v48, v50
	v_permlane32_swap_b32_e32 v49, v51
	v_permlane32_swap_b32_e32 v52, v54
	v_permlane32_swap_b32_e32 v53, v55
	global_store_dwordx4 v[0:1], v[32:35], off offset:1024
	global_store_dwordx4 v[0:1], v[36:39], off offset:1056
	global_store_dwordx4 v[0:1], v[48:51], off offset:1088
	global_store_dwordx4 v[0:1], v[52:55], off offset:1120

; #define LAS __attribute__((address_space(3)))
; __device__ __forceinline__ int opaque_i(int v) { asm volatile("" : "+v"(v)); return v; }
; __device__ __forceinline__ u32x4 pack8(f32x4 a, f32x4 b) { u32x4 w; w.x = pk2(a[0], a[1]); w.y = pk2(a[2], a[3]); w.z = pk2(b[0], b[1]); w.w = pk2(b[2], b[3]); return w; }
; __device__ __forceinline__ int pi32(int i) { return (i & ~12) | ((i & 4) << 1) | ((i & 8) >> 1); }
; __device__ __forceinline__ void attn_moba_unit(Frame& F, const bf16_t* Qh, const bf16_t* Kh, const bf16_t* Vth, const float* KMh, const float slope2, const int qb, bf16_t* AOp) {
;     const int lane = opaque_i(F.lane), r32 = lane & 31, hi = lane >> 5, r32p = pi32(r32), wave = F.wave, q0 = 256 * qb + 32 * wave, q = q0 + r32;
;     LAS unsigned char* ring = F.lds; const unsigned ring_a = (unsigned)(uintptr_t)ring + 16u * (unsigned)lane;
;     bf16x8 qr[4];
; #pragma unroll
;     for (int d0 = 0; d0 < 4; ++d0) qr[d0] = *(const bf16x8*)(Qh + (size_t)q * 64 + 16 * d0 + 8 * hi);
;     f32x16 G = f32x16{};
; #pragma unroll
;     for (int d0 = 0; d0 < 4; ++d0) { u32x4 kw = {0u, 0u, 0u, 0u};
;         if (r32 < 8) { const float* kmp = KMh + r32 * 64 + 16 * d0 + 8 * hi; kw = pack8(*(const f32x4*)kmp, *(const f32x4*)(kmp + 4)); }
;         G = __builtin_amdgcn_mfma_f32_32x32x16_bf16(__builtin_bit_cast(bf16x8, kw), qr[d0], G, 0, 0, 0); }
.LBB0_1285:
	s_mov_b32 s98, 0
	s_and_b32 s0, s94, 2
	v_readlane_b32 s1, v236, 35
	s_or_b32 s0, s0, s1
	s_and_b32 s1, s94, 1
	s_xor_b32 s4, s0, 7
	s_cmp_eq_u32 s1, 0
	s_cselect_b32 s10, s0, s4
	v_mov_b32_e32 v25, v208
	s_lshl_b32 s91, s10, 8
	v_readlane_b32 s0, v236, 7
	s_add_i32 s38, s91, s0
	v_and_b32_e32 v24, 31, v25
	v_ashrrev_i32_e32 v191, 5, v25
	v_or_b32_e32 v160, s38, v24
	v_readlane_b32 s0, v237, 11
	v_lshlrev_b64 v[0:1], 7, v[160:161]
	v_readlane_b32 s1, v237, 12
	v_lshlrev_b32_e32 v48, 3, v191
	v_ashrrev_i32_e32 v49, 31, v48
	v_lshl_add_u64 v[0:1], s[0:1], 0, v[0:1]
	v_lshl_add_u64 v[0:1], v[48:49], 1, v[0:1]
	global_load_dwordx4 v[128:131], v[0:1], off
	global_load_dwordx4 v[132:135], v[0:1], off offset:32
	global_load_dwordx4 v[136:139], v[0:1], off offset:64
	global_load_dwordx4 v[140:143], v[0:1], off offset:96
	v_lshlrev_b32_e32 v0, 8, v24
	v_mov_b32_e32 v1, v161
	v_lshl_add_u64 v[0:1], s[84:85], 0, v[0:1]
	v_cmp_gt_u32_e32 vcc, 8, v24
	v_lshl_add_u64 v[22:23], v[48:49], 2, v[0:1]
	v_mov_b32_e32 v16, 0
	v_mov_b32_e32 v0, 0
	v_mov_b32_e32 v1, 0
	v_mov_b32_e32 v2, 0
	v_mov_b32_e32 v3, 0
	v_mov_b32_e32 v17, 0
	v_mov_b32_e32 v18, 0
	v_mov_b32_e32 v19, 0
	v_mov_b32_e32 v96, 0
	v_mov_b32_e32 v97, 0
	v_mov_b32_e32 v98, 0
	v_mov_b32_e32 v99, 0
	v_mov_b32_e32 v100, 0
	v_mov_b32_e32 v101, 0
	v_mov_b32_e32 v102, 0
	v_mov_b32_e32 v103, 0
	s_and_saveexec_b64 s[0:1], vcc
	s_cbranch_execz .LBB0_1287
	global_load_dwordx4 v[64:67], v[22:23], off
	global_load_dwordx4 v[68:71], v[22:23], off offset:16
	global_load_dwordx4 v[72:75], v[22:23], off offset:64
	global_load_dwordx4 v[76:79], v[22:23], off offset:80
	global_load_dwordx4 v[80:83], v[22:23], off offset:128
	global_load_dwordx4 v[84:87], v[22:23], off offset:144
	global_load_dwordx4 v[88:91], v[22:23], off offset:192
	global_load_dwordx4 v[92:95], v[22:23], off offset:208
	s_waitcnt vmcnt(0)
	v_cvt_pk_bf16_f32 v0, v64, v65
	v_cvt_pk_bf16_f32 v1, v66, v67
	v_cvt_pk_bf16_f32 v2, v68, v69
	v_cvt_pk_bf16_f32 v3, v70, v71
	v_cvt_pk_bf16_f32 v16, v72, v73
	v_cvt_pk_bf16_f32 v17, v74, v75
	v_cvt_pk_bf16_f32 v18, v76, v77
	v_cvt_pk_bf16_f32 v19, v78, v79
	v_cvt_pk_bf16_f32 v96, v80, v81
	v_cvt_pk_bf16_f32 v97, v82, v83
	v_cvt_pk_bf16_f32 v98, v84, v85
	v_cvt_pk_bf16_f32 v99, v86, v87
	v_cvt_pk_bf16_f32 v100, v88, v89
	v_cvt_pk_bf16_f32 v101, v90, v91
	v_cvt_pk_bf16_f32 v102, v92, v93
	v_cvt_pk_bf16_f32 v103, v94, v95

; __device__ __forceinline__ void attn_moba_unit(Frame& F, const bf16_t* Qh, const bf16_t* Kh, const bf16_t* Vth, const float* KMh, const float slope2, const int qb, bf16_t* AOp) {
;     ...
;     for (int T = NT - 1; T >= 0; --T) {
;         if (T >= 2) asm volatile("s_waitcnt vmcnt(4)" ::: "memory"); else if (T == 1) asm volatile("s_waitcnt vmcnt(2)" ::: "memory"); else asm volatile("s_waitcnt vmcnt(0)" ::: "memory");
;         __builtin_amdgcn_s_barrier();
;         if (T >= 3) { const int fs = (slot + 3) & 3; attn_dma_tile(Kh, Vth, T - 3, ring + fs * AT_SLOT, wave, r32, r32p, hi); }
.LBB0_1305:
	s_andn2_b64 vcc, exec, s[0:1]
	s_cbranch_vccnz .LBB0_1307
	s_cmp_lg_u32 s98, 0
	s_mov_b32 s98, 0
	s_cbranch_scc1 .Lmoba_hdr_nodma
	s_lshl_b32 s0, s72, 14
	s_add_i32 s1, s0, 0x8000
	s_and_b32 s1, s1, 0xc000
	s_add_i32 s80, s91, s89
	s_add_i32 s80, s80, 64
	s_add_i32 m0, s1, s33
	s_add_i32 s70, s1, s88
	v_lshl_add_u64 v[80:81], s[80:81], 1, v[178:179]
	s_mov_b64 s[0:1], 0x2000
	v_lshl_add_u64 v[82:83], v[180:181], 0, s[0:1]
	global_load_lds_dwordx4 v[82:83], off
	s_add_i32 m0, s70, 0x2000
	s_nop 0
	global_load_lds_dwordx4 v[80:81], off
.Lmoba_hdr_nodma:
	s_waitcnt vmcnt(4)

; __device__ __forceinline__ float max2_raw(float a, float b) { float d; asm("v_max_f32 %0, %1, %2" : "=v"(d) : "v"(a), "v"(b)); return d; }
; template <int MODE>
; __device__ __forceinline__ void attn_moba_sub(const bf16x8 (&qr)[4], f32x16& O0, f32x16& O1, float& m, float& l, unsigned saddr, int j, int kv0, int q, int q0, int hi, float slope2, bool rowok) {
;     bf16x8 kf[4], vf[2][2];
;     asm volatile("ds_read_b128 %0, %8\n\tds_read_b128 %1, %8 offset:1024\n\tds_read_b128 %2, %8 offset:2048\n\tds_read_b128 %3, %8 offset:3072\n\t"
;                  "ds_read_b128 %4, %9\n\tds_read_b128 %5, %9 offset:1024\n\tds_read_b128 %6, %9 offset:2048\n\tds_read_b128 %7, %9 offset:3072\n\ts_waitcnt lgkmcnt(0)"
;                  : "=&v"(kf[0]), "=&v"(kf[1]), "=&v"(kf[2]), "=&v"(kf[3]), "=&v"(vf[0][0]), "=&v"(vf[0][1]), "=&v"(vf[1][0]), "=&v"(vf[1][1])
;                  : "v"(saddr + (unsigned)j * 4096u), "v"(saddr + 8192u + (unsigned)j * 4096u) : "memory");
;     f32x16 S; const float sbase = slope2 * (float)(kv0 + 8 * hi - q0);
; #pragma unroll
;     for (int r = 0; r < 16; ++r) S[r] = sbase + slope2 * (float)((r & 7) + 16 * (r >> 3));
; #pragma unroll
;     for (int d0 = 0; d0 < 4; ++d0) S = __builtin_amdgcn_mfma_f32_32x32x16_bf16(kf[d0], qr[d0], S, 0, 0, 0);
;     if (MODE == 1) {
; #pragma unroll
;         for (int r = 0; r < 16; ++r) { const int key = kv0 + (r & 7) + 8 * hi + 16 * (r >> 3); if (key > q) S[r] = -INFINITY; }
;     }
;     if (MODE == 2) { if (!rowok) {
; #pragma unroll
;         for (int r = 0; r < 16; ++r) S[r] = -INFINITY; } }
;     float rm = rowmax16_raw(S);
;     { const auto rr = __builtin_amdgcn_permlane32_swap(__float_as_uint(rm), __float_as_uint(rm), false, false); rm = max2_raw(__uint_as_float(rr[0]), __uint_as_float(rr[1])); }
;     if (__any(rm > m)) { const float mn = fmaxf(fmaxf(m, rm), -1e30f); const float alpha = __builtin_amdgcn_exp2f(m - mn); l *= alpha; O0 *= alpha; O1 *= alpha; m = mn; }
.LBB0_1331:
	s_lshr_b32 s0, s92, 2
	s_lshl_b32 s0, 1, s0
	s_and_b32 s1, s0, s79
	s_cmp_eq_u32 s1, 0
	s_cbranch_scc1 .LBB0_1337
	ds_read_b128 v[114:117], v198 offset:4096
	ds_read_b128 v[118:121], v198 offset:5120
	ds_read_b128 v[122:125], v198 offset:6144
	ds_read_b128 v[144:147], v198 offset:7168
	ds_read_b128 v[108:111], v198 offset:12288
	ds_read_b128 v[100:103], v198 offset:13312
	ds_read_b128 v[104:107], v198 offset:14336
	ds_read_b128 v[96:99], v198 offset:15360
	v_add_u32_e32 v113, s89, v195
	s_nop 1
	v_add_u32_e32 v80, 0xe0, v113
	v_cvt_f32_i32_e32 v80, v80
	v_and_b32_e32 v112, s0, v193
	v_cmp_eq_u32_e64 s[70:71], 0, v112
	v_fma_f32 v80, v163, v80, -v196
	s_nop 0
	v_cndmask_b32_e64 v80, v80, v190, s[70:71]
	v_pk_add_f32 v[94:95], v[176:177], v[80:81] op_sel_hi:[1,0]
	v_pk_add_f32 v[92:93], v[174:175], v[80:81] op_sel_hi:[1,0]
	v_pk_add_f32 v[90:91], v[172:173], v[80:81] op_sel_hi:[1,0]
	v_pk_add_f32 v[88:89], v[170:171], v[80:81] op_sel_hi:[1,0]
	v_pk_add_f32 v[86:87], v[168:169], v[80:81] op_sel_hi:[1,0]
	v_pk_add_f32 v[84:85], v[166:167], v[80:81] op_sel_hi:[1,0]
	v_pk_add_f32 v[82:83], v[164:165], v[80:81] op_sel_hi:[1,0]
	v_pk_add_f32 v[80:81], v[162:163], v[80:81] op_sel_hi:[1,0]
	s_waitcnt lgkmcnt(4)
	s_nop 1
	v_mfma_f32_32x32x16_bf16 v[80:95], v[114:117], v[128:131], v[80:95]
	v_mfma_f32_32x32x16_bf16 v[80:95], v[118:121], v[132:135], v[80:95]
	v_mfma_f32_32x32x16_bf16 v[80:95], v[122:125], v[136:139], v[80:95]
	v_mfma_f32_32x32x16_bf16 v[80:95], v[144:147], v[140:143], v[80:95]
	ds_read_b128 v[114:117], v198
	ds_read_b128 v[118:121], v198 offset:1024
	ds_read_b128 v[122:125], v198 offset:2048
	ds_read_b128 v[144:147], v198 offset:3072
	s_nop 7
	v_max3_f32 v222, v80, v81, v82
	v_max3_f32 v223, v83, v84, v85
	v_max3_f32 v224, v86, v87, v88
	v_max3_f32 v222, v222, v223, v224
	v_max3_f32 v223, v89, v90, v91
	v_max3_f32 v224, v92, v93, v94
	v_max3_f32 v223, v223, v224, v95
	v_max_f32_e32 v222, v222, v223
	v_mov_b32_e32 v223, v222
	s_nop 1
	v_permlane32_swap_b32_e32 v222, v223
	v_max_f32_e32 v223, v222, v223
	v_cmp_lt_f32_e32 vcc, 0, v223
	s_cbranch_vccz .Lmoba_m2_1
	v_add_f32_e32 v223, v223, v196
	v_max3_f32 v227, v196, v223, s86
	v_sub_f32_e32 v226, v196, v227
	v_add_f32_e32 v80, v80, v226
	v_add_f32_e32 v81, v81, v226
	v_add_f32_e32 v82, v82, v226
	v_add_f32_e32 v83, v83, v226
	v_add_f32_e32 v84, v84, v226
	v_add_f32_e32 v85, v85, v226
	v_add_f32_e32 v86, v86, v226
	v_add_f32_e32 v87, v87, v226
	v_add_f32_e32 v88, v88, v226
	v_add_f32_e32 v89, v89, v226
	v_add_f32_e32 v90, v90, v226
	v_add_f32_e32 v91, v91, v226
	v_add_f32_e32 v92, v92, v226
	v_add_f32_e32 v93, v93, v226
	v_add_f32_e32 v94, v94, v226
	v_add_f32_e32 v95, v95, v226
	v_exp_f32_e32 v226, v226
	v_mov_b32_e32 v196, v227
	v_mul_f32_e32 v197, v197, v226
	v_pk_mul_f32 v[62:63], v[62:63], v[226:227] op_sel_hi:[1,0]
	v_pk_mul_f32 v[60:61], v[60:61], v[226:227] op_sel_hi:[1,0]
	v_pk_mul_f32 v[58:59], v[58:59], v[226:227] op_sel_hi:[1,0]
	v_pk_mul_f32 v[56:57], v[56:57], v[226:227] op_sel_hi:[1,0]
	v_pk_mul_f32 v[54:55], v[54:55], v[226:227] op_sel_hi:[1,0]
	v_pk_mul_f32 v[52:53], v[52:53], v[226:227] op_sel_hi:[1,0]
	v_pk_mul_f32 v[50:51], v[50:51], v[226:227] op_sel_hi:[1,0]
	v_pk_mul_f32 v[48:49], v[48:49], v[226:227] op_sel_hi:[1,0]
	v_pk_mul_f32 v[78:79], v[78:79], v[226:227] op_sel_hi:[1,0]
	v_pk_mul_f32 v[76:77], v[76:77], v[226:227] op_sel_hi:[1,0]
	v_pk_mul_f32 v[74:75], v[74:75], v[226:227] op_sel_hi:[1,0]
	v_pk_mul_f32 v[72:73], v[72:73], v[226:227] op_sel_hi:[1,0]
	v_pk_mul_f32 v[70:71], v[70:71], v[226:227] op_sel_hi:[1,0]
	v_pk_mul_f32 v[68:69], v[68:69], v[226:227] op_sel_hi:[1,0]
	v_pk_mul_f32 v[66:67], v[66:67], v[226:227] op_sel_hi:[1,0]
	v_pk_mul_f32 v[64:65], v[64:65], v[226:227] op_sel_hi:[1,0]
; template <int MODE>
; __device__ __forceinline__ void attn_moba_sub(const bf16x8 (&qr)[4], f32x16& O0, f32x16& O1, float& m, float& l, unsigned saddr, int j, int kv0, int q, int q0, int hi, float slope2, bool rowok) {
;     bf16x8 kf[4], vf[2][2];
;     asm volatile("ds_read_b128 %0, %8\n\tds_read_b128 %1, %8 offset:1024\n\tds_read_b128 %2, %8 offset:2048\n\tds_read_b128 %3, %8 offset:3072\n\t"
;                  "ds_read_b128 %4, %9\n\tds_read_b128 %5, %9 offset:1024\n\tds_read_b128 %6, %9 offset:2048\n\tds_read_b128 %7, %9 offset:3072\n\ts_waitcnt lgkmcnt(0)"
;                  : "=&v"(kf[0]), "=&v"(kf[1]), "=&v"(kf[2]), "=&v"(kf[3]), "=&v"(vf[0][0]), "=&v"(vf[0][1]), "=&v"(vf[1][0]), "=&v"(vf[1][1])
;                  : "v"(saddr + (unsigned)j * 4096u), "v"(saddr + 8192u + (unsigned)j * 4096u) : "memory");
;     f32x16 S; const float sbase = slope2 * (float)(kv0 + 8 * hi - q0);
; #pragma unroll
;     for (int r = 0; r < 16; ++r) S[r] = sbase + slope2 * (float)((r & 7) + 16 * (r >> 3));
; #pragma unroll
;     for (int d0 = 0; d0 < 4; ++d0) S = __builtin_amdgcn_mfma_f32_32x32x16_bf16(kf[d0], qr[d0], S, 0, 0, 0);
;     if (MODE == 1) {
; #pragma unroll
;         for (int r = 0; r < 16; ++r) { const int key = kv0 + (r & 7) + 8 * hi + 16 * (r >> 3); if (key > q) S[r] = -INFINITY; }
;     }
;     if (MODE == 2) { if (!rowok) {
; #pragma unroll
;         for (int r = 0; r < 16; ++r) S[r] = -INFINITY; } }
;     float rm = rowmax16_raw(S);
;     { const auto rr = __builtin_amdgcn_permlane32_swap(__float_as_uint(rm), __float_as_uint(rm), false, false); rm = max2_raw(__uint_as_float(rr[0]), __uint_as_float(rr[1])); }
;     if (__any(rm > m)) { const float mn = fmaxf(fmaxf(m, rm), -1e30f); const float alpha = __builtin_amdgcn_exp2f(m - mn); l *= alpha; O0 *= alpha; O1 *= alpha; m = mn; }
;     float p[16]; float ps = 0.f;
; #pragma unroll
;     for (int r = 0; r < 16; ++r) { p[r] = __builtin_amdgcn_exp2f(S[r] - m); ps += p[r]; }
;     l += ps;
;     u32x4 w0, w1;
;     w0.x = pk2(p[0], p[1]); w0.y = pk2(p[2], p[3]); w0.z = pk2(p[4], p[5]); w0.w = pk2(p[6], p[7]);
;     w1.x = pk2(p[8], p[9]); w1.y = pk2(p[10], p[11]); w1.z = pk2(p[12], p[13]); w1.w = pk2(p[14], p[15]);
;     const bf16x8 pf0 = __builtin_bit_cast(bf16x8, w0), pf1 = __builtin_bit_cast(bf16x8, w1);
.Lmoba_m2_1:
	v_exp_f32_e32 v80, v80
	v_exp_f32_e32 v81, v81
	v_exp_f32_e32 v82, v82
	v_exp_f32_e32 v83, v83
	v_add_f32_e32 v225, 0, v80
	v_exp_f32_e32 v84, v84
	v_add_f32_e32 v225, v81, v225
	v_exp_f32_e32 v85, v85
	v_add_f32_e32 v225, v82, v225
	v_exp_f32_e32 v86, v86
	v_add_f32_e32 v225, v83, v225
	v_exp_f32_e32 v87, v87
	v_add_f32_e32 v225, v84, v225
	v_exp_f32_e32 v88, v88
	v_add_f32_e32 v225, v85, v225
	v_exp_f32_e32 v89, v89
	v_add_f32_e32 v225, v86, v225
	v_exp_f32_e32 v90, v90
	v_add_f32_e32 v225, v87, v225
	v_exp_f32_e32 v91, v91
	v_cvt_pk_bf16_f32 v80, v80, v81
	v_cvt_pk_bf16_f32 v81, v82, v83
	v_cvt_pk_bf16_f32 v82, v84, v85
	v_cvt_pk_bf16_f32 v83, v86, v87
	v_add_f32_e32 v225, v88, v225
	v_exp_f32_e32 v92, v92
	s_waitcnt lgkmcnt(4)
	v_mfma_f32_32x32x16_bf16 v[48:63], v[108:111], v[80:83], v[48:63]
	v_add_f32_e32 v225, v89, v225
	v_exp_f32_e32 v93, v93
	v_add_f32_e32 v225, v90, v225
	v_exp_f32_e32 v94, v94
	v_add_f32_e32 v225, v91, v225
	v_exp_f32_e32 v95, v95
	v_mfma_f32_32x32x16_bf16 v[64:79], v[100:103], v[80:83], v[64:79]
	v_add_f32_e32 v225, v92, v225
	v_add_f32_e32 v225, v93, v225
	v_add_f32_e32 v225, v94, v225
	v_add_f32_e32 v225, v95, v225
	v_cvt_pk_bf16_f32 v84, v88, v89
	v_cvt_pk_bf16_f32 v85, v90, v91
	v_cvt_pk_bf16_f32 v86, v92, v93
	v_cvt_pk_bf16_f32 v87, v94, v95
	v_add_f32_e32 v112, v197, v225
	s_nop 0
	v_mfma_f32_32x32x16_bf16 v[48:63], v[104:107], v[84:87], v[48:63]
	v_mfma_f32_32x32x16_bf16 v[64:79], v[96:99], v[84:87], v[64:79]
	ds_read_b128 v[108:111], v198 offset:8192
	ds_read_b128 v[100:103], v198 offset:9216
	ds_read_b128 v[104:107], v198 offset:10240
	ds_read_b128 v[96:99], v198 offset:11264
	v_add_u32_e32 v80, 0xc0, v113
	v_cvt_f32_i32_e32 v80, v80
	v_fma_f32 v80, v163, v80, -v196
	v_cndmask_b32_e64 v80, v80, v190, s[70:71]
	v_pk_add_f32 v[94:95], v[176:177], v[80:81] op_sel_hi:[1,0]
	v_pk_add_f32 v[92:93], v[174:175], v[80:81] op_sel_hi:[1,0]
	v_pk_add_f32 v[90:91], v[172:173], v[80:81] op_sel_hi:[1,0]
	v_pk_add_f32 v[88:89], v[170:171], v[80:81] op_sel_hi:[1,0]
	v_pk_add_f32 v[86:87], v[168:169], v[80:81] op_sel_hi:[1,0]
	v_pk_add_f32 v[84:85], v[166:167], v[80:81] op_sel_hi:[1,0]
	v_pk_add_f32 v[82:83], v[164:165], v[80:81] op_sel_hi:[1,0]
	v_pk_add_f32 v[80:81], v[162:163], v[80:81] op_sel_hi:[1,0]
	s_waitcnt lgkmcnt(4)
	s_nop 1
	v_mfma_f32_32x32x16_bf16 v[80:95], v[114:117], v[128:131], v[80:95]
	v_mfma_f32_32x32x16_bf16 v[80:95], v[118:121], v[132:135], v[80:95]
	v_mfma_f32_32x32x16_bf16 v[80:95], v[122:125], v[136:139], v[80:95]
	v_mfma_f32_32x32x16_bf16 v[80:95], v[144:147], v[140:143], v[80:95]
	s_nop 11
	v_max3_f32 v222, v80, v81, v82
	v_max3_f32 v223, v83, v84, v85
	v_max3_f32 v224, v86, v87, v88
	v_max3_f32 v222, v222, v223, v224
	v_max3_f32 v223, v89, v90, v91
	v_max3_f32 v224, v92, v93, v94
	v_max3_f32 v223, v223, v224, v95
	v_max_f32_e32 v222, v222, v223
	v_mov_b32_e32 v223, v222
	s_nop 1
	v_permlane32_swap_b32_e32 v222, v223
	v_max_f32_e32 v223, v222, v223
	v_cmp_lt_f32_e32 vcc, 0, v223
	s_cbranch_vccz .Lmoba_m2_2
	v_add_f32_e32 v223, v223, v196
	v_max3_f32 v227, v196, v223, s86
	v_sub_f32_e32 v226, v196, v227
	v_add_f32_e32 v80, v80, v226
	v_add_f32_e32 v81, v81, v226
	v_add_f32_e32 v82, v82, v226
	v_add_f32_e32 v83, v83, v226
	v_add_f32_e32 v84, v84, v226
	v_add_f32_e32 v85, v85, v226
	v_add_f32_e32 v86, v86, v226
	v_add_f32_e32 v87, v87, v226
	v_add_f32_e32 v88, v88, v226
	v_add_f32_e32 v89, v89, v226
	v_add_f32_e32 v90, v90, v226
	v_add_f32_e32 v91, v91, v226
	v_add_f32_e32 v92, v92, v226
	v_add_f32_e32 v93, v93, v226
	v_add_f32_e32 v94, v94, v226
	v_add_f32_e32 v95, v95, v226
	v_exp_f32_e32 v226, v226
	v_mov_b32_e32 v196, v227
	v_mul_f32_e32 v112, v226, v112
	v_pk_mul_f32 v[62:63], v[62:63], v[226:227] op_sel_hi:[1,0]
	v_pk_mul_f32 v[60:61], v[60:61], v[226:227] op_sel_hi:[1,0]
	v_pk_mul_f32 v[58:59], v[58:59], v[226:227] op_sel_hi:[1,0]
	v_pk_mul_f32 v[56:57], v[56:57], v[226:227] op_sel_hi:[1,0]
	v_pk_mul_f32 v[54:55], v[54:55], v[226:227] op_sel_hi:[1,0]
	v_pk_mul_f32 v[52:53], v[52:53], v[226:227] op_sel_hi:[1,0]
	v_pk_mul_f32 v[50:51], v[50:51], v[226:227] op_sel_hi:[1,0]
	v_pk_mul_f32 v[48:49], v[48:49], v[226:227] op_sel_hi:[1,0]
	v_pk_mul_f32 v[78:79], v[78:79], v[226:227] op_sel_hi:[1,0]
	v_pk_mul_f32 v[76:77], v[76:77], v[226:227] op_sel_hi:[1,0]
	v_pk_mul_f32 v[74:75], v[74:75], v[226:227] op_sel_hi:[1,0]
	v_pk_mul_f32 v[72:73], v[72:73], v[226:227] op_sel_hi:[1,0]
	v_pk_mul_f32 v[70:71], v[70:71], v[226:227] op_sel_hi:[1,0]
	v_pk_mul_f32 v[68:69], v[68:69], v[226:227] op_sel_hi:[1,0]
	v_pk_mul_f32 v[66:67], v[66:67], v[226:227] op_sel_hi:[1,0]
	v_pk_mul_f32 v[64:65], v[64:65], v[226:227] op_sel_hi:[1,0]

; __device__ __forceinline__ unsigned pk2(float lo, float hi) { const f32x2_pk v = {lo, hi}; return __builtin_bit_cast(unsigned, __builtin_convertvector(v, bf16x2)); }
; __device__ __forceinline__ void attn_moba_unit(Frame& F, const bf16_t* Qh, const bf16_t* Kh, const bf16_t* Vth, const float* KMh, const float slope2, const int qb, bf16_t* AOp) {
;     ...
;     const float linv = 1.f / (l + __shfl_xor(l, 32));
;     bf16_t* orow = AOp + (size_t)q * DM;
; #pragma unroll
;     for (int g = 0; g < 4; ++g) { u32x2 w;
;         w.x = pk2(O0[4 * g] * linv, O0[4 * g + 1] * linv); w.y = pk2(O0[4 * g + 2] * linv, O0[4 * g + 3] * linv); *(u32x2*)(orow + 8 * g + 4 * hi) = w;
;         w.x = pk2(O1[4 * g] * linv, O1[4 * g + 1] * linv); w.y = pk2(O1[4 * g + 2] * linv, O1[4 * g + 3] * linv); *(u32x2*)(orow + 32 + 8 * g + 4 * hi) = w; }
.Lmoba_epi:
	ds_bpermute_b32 v0, v192, v116
	s_add_i32 s94, s94, 1
	s_cmp_eq_u32 s94, 4
	s_mov_b32 s14, 0xff800000
	s_waitcnt lgkmcnt(0)
	v_add_f32_e32 v0, v116, v0
	v_div_scale_f32 v1, s[0:1], v0, v0, 1.0
	v_rcp_f32_e32 v2, v1
	s_nop 0
	v_fma_f32 v3, -v1, v2, 1.0
	v_fmac_f32_e32 v2, v3, v2
	v_div_scale_f32 v3, vcc, 1.0, v0, 1.0
	v_mul_f32_e32 v4, v3, v2
	v_fma_f32 v5, -v1, v4, v3
	v_fmac_f32_e32 v4, v5, v2
	v_fma_f32 v1, -v1, v4, v3
	v_div_fmas_f32 v1, v1, v2, v4
	v_lshlrev_b64 v[2:3], 11, v[160:161]
	v_lshlrev_b32_e32 v4, 3, v191
	v_div_fixup_f32 v0, v1, v0, 1.0
	v_lshl_add_u64 v[2:3], s[76:77], 0, v[2:3]
	v_ashrrev_i32_e32 v5, 31, v4
	v_lshl_add_u64 v[2:3], v[4:5], 1, v[2:3]
	v_pk_mul_f32 v[96:97], v[96:97], v[0:1] op_sel_hi:[1,0]
	v_pk_mul_f32 v[98:99], v[98:99], v[0:1] op_sel_hi:[1,0]
	v_pk_mul_f32 v[100:101], v[100:101], v[0:1] op_sel_hi:[1,0]
	v_pk_mul_f32 v[102:103], v[102:103], v[0:1] op_sel_hi:[1,0]
	v_pk_mul_f32 v[104:105], v[104:105], v[0:1] op_sel_hi:[1,0]
	v_pk_mul_f32 v[106:107], v[106:107], v[0:1] op_sel_hi:[1,0]
	v_pk_mul_f32 v[108:109], v[108:109], v[0:1] op_sel_hi:[1,0]
	v_pk_mul_f32 v[110:111], v[110:111], v[0:1] op_sel_hi:[1,0]
	v_pk_mul_f32 v[80:81], v[80:81], v[0:1] op_sel_hi:[1,0]
	v_pk_mul_f32 v[82:83], v[82:83], v[0:1] op_sel_hi:[1,0]
	v_pk_mul_f32 v[84:85], v[84:85], v[0:1] op_sel_hi:[1,0]
	v_pk_mul_f32 v[86:87], v[86:87], v[0:1] op_sel_hi:[1,0]
	v_pk_mul_f32 v[88:89], v[88:89], v[0:1] op_sel_hi:[1,0]
	v_pk_mul_f32 v[90:91], v[90:91], v[0:1] op_sel_hi:[1,0]
	v_pk_mul_f32 v[92:93], v[92:93], v[0:1] op_sel_hi:[1,0]
	v_pk_mul_f32 v[94:95], v[94:95], v[0:1] op_sel_hi:[1,0]
	v_cvt_pk_bf16_f32 v96, v96, v97
	v_cvt_pk_bf16_f32 v97, v98, v99
	v_cvt_pk_bf16_f32 v98, v100, v101
	v_cvt_pk_bf16_f32 v99, v102, v103
	v_cvt_pk_bf16_f32 v100, v104, v105
	v_cvt_pk_bf16_f32 v101, v106, v107
	v_cvt_pk_bf16_f32 v102, v108, v109
	v_cvt_pk_bf16_f32 v103, v110, v111
	v_cvt_pk_bf16_f32 v80, v80, v81
	v_cvt_pk_bf16_f32 v81, v82, v83
	v_cvt_pk_bf16_f32 v82, v84, v85
	v_cvt_pk_bf16_f32 v83, v86, v87
	v_cvt_pk_bf16_f32 v84, v88, v89
	v_cvt_pk_bf16_f32 v85, v90, v91
	v_cvt_pk_bf16_f32 v86, v92, v93
	v_cvt_pk_bf16_f32 v87, v94, v95
	s_nop 1
	v_permlane32_swap_b32_e32 v96, v98
	v_permlane32_swap_b32_e32 v97, v99
	v_permlane32_swap_b32_e32 v100, v102
	v_permlane32_swap_b32_e32 v101, v103
	v_permlane32_swap_b32_e32 v80, v82
	v_permlane32_swap_b32_e32 v81, v83
	v_permlane32_swap_b32_e32 v84, v86
	v_permlane32_swap_b32_e32 v85, v87
	global_store_dwordx4 v[2:3], v[96:99], off offset:1024
	global_store_dwordx4 v[2:3], v[100:103], off offset:1056
	global_store_dwordx4 v[2:3], v[80:83], off offset:1088
	global_store_dwordx4 v[2:3], v[84:87], off offset:1120
	s_waitcnt vmcnt(0) lgkmcnt(0)
	s_barrier
	s_cbranch_scc0 .LBB0_1285
	s_branch .LBB0_1277

; __device__ __forceinline__ unsigned pk2(float lo, float hi) { const f32x2_pk v = {lo, hi}; return __builtin_bit_cast(unsigned, __builtin_convertvector(v, bf16x2)); }
; __device__ __forceinline__ float bf_lo(unsigned u) { return __uint_as_float(u << 16); }
; __device__ __forceinline__ float bf_hi(unsigned u) { return __uint_as_float(u & 0xffff0000u); }
; __device__ __forceinline__ void phase_pool(Frame& F, const bf16_t* XC, const bf16_t* PWT, const float* pool_scale, bf16_t* AO) {
;     ...
;             const u32x4 self = *(const u32x4*)(XC + (size_t)t * 512 + c0);
;             float s[8] = {0.f, 0.f, 0.f, 0.f, 0.f, 0.f, 0.f, 0.f};
;             for (int i = 0; i < cnt; ++i) { const u32x4 x = *(const u32x4*)(XC + (size_t)(t - i) * 512 + c0);
;                 s[0] += bf_lo(x.x); s[1] += bf_hi(x.x); s[2] += bf_lo(x.y); s[3] += bf_hi(x.y); s[4] += bf_lo(x.z); s[5] += bf_hi(x.z); s[6] += bf_lo(x.w); s[7] += bf_hi(x.w); }
;             u32x4 pa; pa.x = pk2(s[0] * rc - bf_lo(self.x), s[1] * rc - bf_hi(self.x)); pa.y = pk2(s[2] * rc - bf_lo(self.y), s[3] * rc - bf_hi(self.y));
;             pa.z = pk2(s[4] * rc - bf_lo(self.z), s[5] * rc - bf_hi(self.z)); pa.w = pk2(s[6] * rc - bf_lo(self.w), s[7] * rc - bf_hi(self.w));
;             const bf16x8 af = __builtin_bit_cast(bf16x8, pa);
; #pragma unroll
;             for (int nb = 0; nb < 4; ++nb) { const bf16x8 bfr = *(const bf16x8*)(PWT + ((size_t)g * 128 + nb * 32 + r32) * 128 + kk * 16 + hi * 8);
;                 acc[nb] = __builtin_amdgcn_mfma_f32_32x32x16_bf16(af, bfr, acc[nb], 0, 0, 0); }
.LBB0_1345:
	ds_read_b128 v[98:101], v92
	v_add_co_u32_e32 v77, vcc, 1, v77
	v_add_u32_e32 v92, 0xfffffef0, v92
	s_or_b64 s[4:5], vcc, s[4:5]
	s_waitcnt lgkmcnt(0)
	v_lshlrev_b32_e32 v102, 16, v98
	v_and_b32_e32 v103, 0xffff0000, v98
	v_lshlrev_b32_e32 v98, 16, v99
	v_and_b32_e32 v99, 0xffff0000, v99
	v_lshlrev_b32_e32 v104, 16, v100
	v_and_b32_e32 v105, 0xffff0000, v100
	v_lshlrev_b32_e32 v100, 16, v101
	v_and_b32_e32 v101, 0xffff0000, v101
	v_pk_add_f32 v[90:91], v[90:91], v[102:103]
	v_pk_add_f32 v[88:89], v[88:89], v[98:99]
	v_pk_add_f32 v[86:87], v[86:87], v[104:105]
	v_pk_add_f32 v[84:85], v[84:85], v[100:101]
	s_andn2_b64 exec, exec, s[4:5]
	s_cbranch_execnz .LBB0_1345
	s_or_b64 exec, exec, s[4:5]
	v_lshlrev_b32_e32 v108, 16, v66
	v_and_b32_e32 v109, 0xffff0000, v66
	v_lshlrev_b32_e32 v66, 16, v67
	v_and_b32_e32 v67, 0xffff0000, v67
	v_pk_fma_f32 v[84:85], v[74:75], v[84:85], v[66:67] neg_lo:[0,0,1] neg_hi:[0,0,1]
	v_lshlrev_b32_e32 v106, 16, v64
	v_and_b32_e32 v107, 0xffff0000, v64
	v_lshlrev_b32_e32 v64, 16, v65
	v_and_b32_e32 v65, 0xffff0000, v65
	v_cvt_pk_bf16_f32 v67, v84, v85
	v_pk_fma_f32 v[88:89], v[74:75], v[88:89], v[64:65] neg_lo:[0,0,1] neg_hi:[0,0,1]
	s_nop 0
	v_cvt_pk_bf16_f32 v65, v88, v89
	v_pk_fma_f32 v[90:91], v[74:75], v[90:91], v[106:107] neg_lo:[0,0,1] neg_hi:[0,0,1]
	v_pk_fma_f32 v[86:87], v[74:75], v[86:87], v[108:109] neg_lo:[0,0,1] neg_hi:[0,0,1]
	v_cvt_pk_bf16_f32 v64, v90, v91
	v_cvt_pk_bf16_f32 v66, v86, v87
	s_add_i32 s21, s21, 1
	s_cmp_eq_u32 s21, 8
	v_lshl_add_u64 v[82:83], v[82:83], 0, 32
	s_waitcnt vmcnt(3)
	v_mfma_f32_32x32x16_bf16 v[48:63], v[164:167], v[64:67], v[48:63]
	s_waitcnt vmcnt(2)
	v_mfma_f32_32x32x16_bf16 v[32:47], v[168:171], v[64:67], v[32:47]
	s_waitcnt vmcnt(1)
	v_mfma_f32_32x32x16_bf16 v[16:31], v[172:175], v[64:67], v[16:31]
	s_waitcnt vmcnt(0)
	v_mfma_f32_32x32x16_bf16 v[0:15], v[176:179], v[64:67], v[0:15]
	s_cbranch_scc0 .LBB0_1344
; __device__ __forceinline__ unsigned f2bf(float f) { unsigned u = __builtin_bit_cast(unsigned, f); return (u + 0x7fffu + ((u >> 16) & 1u)) >> 16; }
; __device__ __forceinline__ void phase_pool(Frame& F, const bf16_t* XC, const bf16_t* PWT, const float* pool_scale, bf16_t* AO) {
;     ...
; #pragma unroll
;         for (int nb = 0; nb < 4; ++nb) { const int col = g * 128 + nb * 32 + r32; const float sc = pool_scale[col];
; #pragma unroll
;             for (int r = 0; r < 16; ++r) { const int row = (r & 3) + 8 * (r >> 2) + 4 * hi; AO[(size_t)(t0 + row) * DM + col] = (bf16_t)f2bf(acc[nb][r] * sc); } }
	v_readlane_b32 s36, v237, 27
	v_readlane_b32 s37, v237, 28
	v_readlane_b32 s4, v237, 45
	v_readlane_b32 s5, v237, 46
	v_add_u32_e32 v66, s20, v69
	v_add_u32_e32 v64, s19, v94
	s_lshl_b32 s0, s20, 1
	v_lshl_add_u32 v74, v69, 2, s0
	v_lshlrev_b32_e32 v66, 2, v66
	v_ashrrev_i32_e32 v65, 31, v64
	v_mov_b32_e32 v75, 0
	v_lshlrev_b64 v[64:65], 11, v[64:65]
	global_load_dwordx4 v[100:103], v66, s[36:37]
	global_load_dwordx4 v[104:107], v66, s[36:37] offset:32
	global_load_dwordx4 v[108:111], v66, s[36:37] offset:64
	global_load_dwordx4 v[112:115], v66, s[36:37] offset:96
	global_load_dwordx4 v[116:119], v66, s[36:37] offset:128
	global_load_dwordx4 v[120:123], v66, s[36:37] offset:160
	global_load_dwordx4 v[124:127], v66, s[36:37] offset:192
	global_load_dwordx4 v[128:131], v66, s[36:37] offset:224
	global_load_dwordx4 v[132:135], v66, s[36:37] offset:256
	global_load_dwordx4 v[136:139], v66, s[36:37] offset:288
	global_load_dwordx4 v[140:143], v66, s[36:37] offset:320
	global_load_dwordx4 v[144:147], v66, s[36:37] offset:352
	global_load_dwordx4 v[148:151], v66, s[36:37] offset:384
	global_load_dwordx4 v[152:155], v66, s[36:37] offset:416
	global_load_dwordx4 v[156:159], v66, s[36:37] offset:448
	global_load_dwordx4 v[160:163], v66, s[36:37] offset:480
	v_lshl_add_u64 v[64:65], s[4:5], 0, v[64:65]
	v_lshl_add_u64 v[64:65], v[64:65], 0, v[74:75]
	v_readlane_b32 s38, v237, 29
	v_readlane_b32 s39, v237, 30
	v_readlane_b32 s40, v237, 31
	v_readlane_b32 s41, v237, 32
	v_readlane_b32 s42, v237, 33
	v_readlane_b32 s43, v237, 34
	v_readlane_b32 s44, v237, 35
	v_readlane_b32 s45, v237, 36
	v_readlane_b32 s46, v237, 37
	v_readlane_b32 s47, v237, 38
	v_readlane_b32 s48, v237, 39
	v_readlane_b32 s49, v237, 40
	v_readlane_b32 s50, v237, 41
	v_readlane_b32 s51, v237, 42
	s_waitcnt vmcnt(12)
	v_pk_mul_f32 v[48:49], v[48:49], v[100:101]
	v_pk_mul_f32 v[50:51], v[50:51], v[102:103]
	v_pk_mul_f32 v[52:53], v[52:53], v[104:105]
	v_pk_mul_f32 v[54:55], v[54:55], v[106:107]
	v_pk_mul_f32 v[56:57], v[56:57], v[108:109]
	v_pk_mul_f32 v[58:59], v[58:59], v[110:111]
	v_pk_mul_f32 v[60:61], v[60:61], v[112:113]
	v_pk_mul_f32 v[62:63], v[62:63], v[114:115]
	v_cvt_pk_bf16_f32 v48, v48, v49
	v_cvt_pk_bf16_f32 v49, v50, v51
	v_cvt_pk_bf16_f32 v50, v52, v53
	v_cvt_pk_bf16_f32 v51, v54, v55
	v_cvt_pk_bf16_f32 v52, v56, v57
	v_cvt_pk_bf16_f32 v53, v58, v59
	v_cvt_pk_bf16_f32 v54, v60, v61
	v_cvt_pk_bf16_f32 v55, v62, v63
	s_nop 1
	v_permlane32_swap_b32_e32 v48, v50
	v_permlane32_swap_b32_e32 v49, v51
	v_permlane32_swap_b32_e32 v52, v54
	v_permlane32_swap_b32_e32 v53, v55
	global_store_dwordx4 v[64:65], v[48:51], off
	global_store_dwordx4 v[64:65], v[52:55], off offset:32
	s_waitcnt vmcnt(10)
	v_pk_mul_f32 v[32:33], v[32:33], v[116:117]
	v_pk_mul_f32 v[34:35], v[34:35], v[118:119]
	v_pk_mul_f32 v[36:37], v[36:37], v[120:121]
	v_pk_mul_f32 v[38:39], v[38:39], v[122:123]
	v_pk_mul_f32 v[40:41], v[40:41], v[124:125]
	v_pk_mul_f32 v[42:43], v[42:43], v[126:127]
	v_pk_mul_f32 v[44:45], v[44:45], v[128:129]
	v_pk_mul_f32 v[46:47], v[46:47], v[130:131]
	v_cvt_pk_bf16_f32 v32, v32, v33
	v_cvt_pk_bf16_f32 v33, v34, v35
	v_cvt_pk_bf16_f32 v34, v36, v37
	v_cvt_pk_bf16_f32 v35, v38, v39
	v_cvt_pk_bf16_f32 v36, v40, v41
	v_cvt_pk_bf16_f32 v37, v42, v43
	v_cvt_pk_bf16_f32 v38, v44, v45
	v_cvt_pk_bf16_f32 v39, v46, v47
	s_nop 1
	v_permlane32_swap_b32_e32 v32, v34
	v_permlane32_swap_b32_e32 v33, v35
	v_permlane32_swap_b32_e32 v36, v38
	v_permlane32_swap_b32_e32 v37, v39
	global_store_dwordx4 v[64:65], v[32:35], off offset:64
	global_store_dwordx4 v[64:65], v[36:39], off offset:96
	s_waitcnt vmcnt(8)
	v_pk_mul_f32 v[16:17], v[16:17], v[132:133]
	v_pk_mul_f32 v[18:19], v[18:19], v[134:135]
	v_pk_mul_f32 v[20:21], v[20:21], v[136:137]
	v_pk_mul_f32 v[22:23], v[22:23], v[138:139]
	v_pk_mul_f32 v[24:25], v[24:25], v[140:141]
	v_pk_mul_f32 v[26:27], v[26:27], v[142:143]
	v_pk_mul_f32 v[28:29], v[28:29], v[144:145]
	v_pk_mul_f32 v[30:31], v[30:31], v[146:147]
	v_cvt_pk_bf16_f32 v16, v16, v17
	v_cvt_pk_bf16_f32 v17, v18, v19
	v_cvt_pk_bf16_f32 v18, v20, v21
	v_cvt_pk_bf16_f32 v19, v22, v23
	v_cvt_pk_bf16_f32 v20, v24, v25
	v_cvt_pk_bf16_f32 v21, v26, v27
	v_cvt_pk_bf16_f32 v22, v28, v29
	v_cvt_pk_bf16_f32 v23, v30, v31
	s_nop 1
	v_permlane32_swap_b32_e32 v16, v18
	v_permlane32_swap_b32_e32 v17, v19
	v_permlane32_swap_b32_e32 v20, v22
	v_permlane32_swap_b32_e32 v21, v23
	global_store_dwordx4 v[64:65], v[16:19], off offset:128
	global_store_dwordx4 v[64:65], v[20:23], off offset:160
	s_waitcnt vmcnt(6)
	v_pk_mul_f32 v[0:1], v[0:1], v[148:149]
	v_pk_mul_f32 v[2:3], v[2:3], v[150:151]
	v_pk_mul_f32 v[4:5], v[4:5], v[152:153]
	v_pk_mul_f32 v[6:7], v[6:7], v[154:155]
	v_pk_mul_f32 v[8:9], v[8:9], v[156:157]
	v_pk_mul_f32 v[10:11], v[10:11], v[158:159]
	v_pk_mul_f32 v[12:13], v[12:13], v[160:161]
	v_pk_mul_f32 v[14:15], v[14:15], v[162:163]
	v_cvt_pk_bf16_f32 v0, v0, v1
	v_cvt_pk_bf16_f32 v1, v2, v3
	v_cvt_pk_bf16_f32 v2, v4, v5
	v_cvt_pk_bf16_f32 v3, v6, v7
	v_cvt_pk_bf16_f32 v4, v8, v9
	v_cvt_pk_bf16_f32 v5, v10, v11
	v_cvt_pk_bf16_f32 v6, v12, v13
	v_cvt_pk_bf16_f32 v7, v14, v15
	s_nop 1
	v_permlane32_swap_b32_e32 v0, v2
	v_permlane32_swap_b32_e32 v1, v3
	v_permlane32_swap_b32_e32 v4, v6
	v_permlane32_swap_b32_e32 v5, v7
	global_store_dwordx4 v[64:65], v[0:3], off offset:192
	global_store_dwordx4 v[64:65], v[4:7], off offset:224
	s_add_i32 s6, s6, s7
	s_cmpk_gt_i32 s6, 0xfff
	s_cbranch_scc0 .LBB0_1343
